# compress-finalize LDS fill: sixteen loads issued back to back with counted waits instead of a wait after each load
# speedup vs baseline: 1.0155x; 1.0007x over previous
.LBB0_968:
	global_load_dwordx4 v[64:67], v[4:5], off
	v_add_co_u32_e32 v6, vcc, 0x2000, v4
	s_nop 1
	v_addc_co_u32_e32 v7, vcc, 0, v5, vcc
	global_load_dwordx4 v[68:71], v[6:7], off
	v_add_co_u32_e32 v6, vcc, 0x4000, v4
	s_nop 1
	v_addc_co_u32_e32 v7, vcc, 0, v5, vcc
	global_load_dwordx4 v[72:75], v[6:7], off
	v_add_co_u32_e32 v6, vcc, 0x6000, v4
	s_nop 1
	v_addc_co_u32_e32 v7, vcc, 0, v5, vcc
	global_load_dwordx4 v[76:79], v[6:7], off
	v_add_co_u32_e32 v6, vcc, 0x8000, v4
	s_nop 1
	v_addc_co_u32_e32 v7, vcc, 0, v5, vcc
	global_load_dwordx4 v[80:83], v[6:7], off
	v_add_co_u32_e32 v6, vcc, 0xa000, v4
	s_nop 1
	v_addc_co_u32_e32 v7, vcc, 0, v5, vcc
	global_load_dwordx4 v[84:87], v[6:7], off
	v_add_co_u32_e32 v6, vcc, 0xc000, v4
	s_nop 1
	v_addc_co_u32_e32 v7, vcc, 0, v5, vcc
	global_load_dwordx4 v[88:91], v[6:7], off
	v_add_co_u32_e32 v6, vcc, 0xe000, v4
	s_nop 1
	v_addc_co_u32_e32 v7, vcc, 0, v5, vcc
	global_load_dwordx4 v[92:95], v[6:7], off
	v_add_co_u32_e32 v6, vcc, 0x10000, v4
	s_nop 1
	v_addc_co_u32_e32 v7, vcc, 0, v5, vcc
	global_load_dwordx4 v[96:99], v[6:7], off
	v_add_co_u32_e32 v6, vcc, 0x12000, v4
	s_nop 1
	v_addc_co_u32_e32 v7, vcc, 0, v5, vcc
	global_load_dwordx4 v[100:103], v[6:7], off
	v_add_co_u32_e32 v6, vcc, 0x14000, v4
	s_nop 1
	v_addc_co_u32_e32 v7, vcc, 0, v5, vcc
	global_load_dwordx4 v[104:107], v[6:7], off
	v_add_co_u32_e32 v6, vcc, 0x16000, v4
	s_nop 1
	v_addc_co_u32_e32 v7, vcc, 0, v5, vcc
	global_load_dwordx4 v[108:111], v[6:7], off
	v_add_co_u32_e32 v6, vcc, 0x18000, v4
	s_nop 1
	v_addc_co_u32_e32 v7, vcc, 0, v5, vcc
	global_load_dwordx4 v[112:115], v[6:7], off
	v_add_co_u32_e32 v6, vcc, 0x1a000, v4
	s_nop 1
	v_addc_co_u32_e32 v7, vcc, 0, v5, vcc
	global_load_dwordx4 v[116:119], v[6:7], off
	v_add_co_u32_e32 v6, vcc, 0x1c000, v4
	s_nop 1
	v_addc_co_u32_e32 v7, vcc, 0, v5, vcc
	global_load_dwordx4 v[120:123], v[6:7], off
	v_add_co_u32_e32 v6, vcc, 0x1e000, v4
	s_nop 1
	v_addc_co_u32_e32 v7, vcc, 0, v5, vcc
	global_load_dwordx4 v[124:127], v[6:7], off
	s_waitcnt vmcnt(15)
	ds_write_b128 v3, v[64:67]
	s_waitcnt vmcnt(14)
	ds_write_b128 v3, v[68:71] offset:8192
	s_waitcnt vmcnt(13)
	ds_write_b128 v3, v[72:75] offset:16384
	s_waitcnt vmcnt(12)
	ds_write_b128 v3, v[76:79] offset:24576
	v_add_u32_e32 v3, 0x8000, v3
	s_waitcnt vmcnt(11)
	ds_write_b128 v3, v[80:83]
	s_waitcnt vmcnt(10)
	ds_write_b128 v3, v[84:87] offset:8192
	s_waitcnt vmcnt(9)
	ds_write_b128 v3, v[88:91] offset:16384
	s_waitcnt vmcnt(8)
	ds_write_b128 v3, v[92:95] offset:24576
	v_add_u32_e32 v3, 0x8000, v3
	s_waitcnt vmcnt(7)
	ds_write_b128 v3, v[96:99]
	s_waitcnt vmcnt(6)
	ds_write_b128 v3, v[100:103] offset:8192
	s_waitcnt vmcnt(5)
	ds_write_b128 v3, v[104:107] offset:16384
	s_waitcnt vmcnt(4)
	ds_write_b128 v3, v[108:111] offset:24576
	v_add_u32_e32 v3, 0x8000, v3
	s_waitcnt vmcnt(3)
	ds_write_b128 v3, v[112:115]
	s_waitcnt vmcnt(2)
	ds_write_b128 v3, v[116:119] offset:8192
	s_waitcnt vmcnt(1)
	ds_write_b128 v3, v[120:123] offset:16384
	s_waitcnt vmcnt(0)
	ds_write_b128 v3, v[124:127] offset:24576
